# indexer pass B only: two histogram keys per exec round-trip (masks in two SGPR pairs, full exec kept in vcc)
# baseline (speedup 1.0000x reference)
.Lpb_go:
	s_mov_b64 vcc, exec
	v_cmp_eq_u32_sdwa s[38:39], v208, v4 src0_sel:BYTE_1 src1_sel:DWORD
	v_cmp_eq_u32_sdwa s[0:1], v208, v4 src0_sel:BYTE_3 src1_sel:DWORD
	v_and_b32_e32 v8, 0xff, v208
	v_bfe_u32 v9, v208, 16, 8
	v_lshl_add_u32 v8, v8, 2, v6
	v_lshl_add_u32 v9, v9, 2, v6
	s_mov_b64 exec, s[38:39]
	ds_add_u32 v8, v224
	s_mov_b64 exec, s[0:1]
	ds_add_u32 v9, v224
	s_mov_b64 exec, vcc
	v_cmp_eq_u32_sdwa s[38:39], v209, v4 src0_sel:BYTE_1 src1_sel:DWORD
	v_cmp_eq_u32_sdwa s[0:1], v209, v4 src0_sel:BYTE_3 src1_sel:DWORD
	v_and_b32_e32 v8, 0xff, v209
	v_bfe_u32 v9, v209, 16, 8
	v_lshl_add_u32 v8, v8, 2, v6
	v_lshl_add_u32 v9, v9, 2, v6
	s_mov_b64 exec, s[38:39]
	ds_add_u32 v8, v224
	s_mov_b64 exec, s[0:1]
	ds_add_u32 v9, v224
	s_mov_b64 exec, vcc
	v_cmp_eq_u32_sdwa s[38:39], v210, v4 src0_sel:BYTE_1 src1_sel:DWORD
	v_cmp_eq_u32_sdwa s[0:1], v210, v4 src0_sel:BYTE_3 src1_sel:DWORD
	v_and_b32_e32 v8, 0xff, v210
	v_bfe_u32 v9, v210, 16, 8
	v_lshl_add_u32 v8, v8, 2, v6
	v_lshl_add_u32 v9, v9, 2, v6
	s_mov_b64 exec, s[38:39]
	ds_add_u32 v8, v224
	s_mov_b64 exec, s[0:1]
	ds_add_u32 v9, v224
	s_mov_b64 exec, vcc
	v_cmp_eq_u32_sdwa s[38:39], v211, v4 src0_sel:BYTE_1 src1_sel:DWORD
	v_cmp_eq_u32_sdwa s[0:1], v211, v4 src0_sel:BYTE_3 src1_sel:DWORD
	v_and_b32_e32 v8, 0xff, v211
	v_bfe_u32 v9, v211, 16, 8
	v_lshl_add_u32 v8, v8, 2, v6
	v_lshl_add_u32 v9, v9, 2, v6
	s_mov_b64 exec, s[38:39]
	ds_add_u32 v8, v224
	s_mov_b64 exec, s[0:1]
	ds_add_u32 v9, v224
	s_mov_b64 exec, vcc
	v_cmp_eq_u32_sdwa s[38:39], v204, v4 src0_sel:BYTE_1 src1_sel:DWORD
	v_cmp_eq_u32_sdwa s[0:1], v204, v4 src0_sel:BYTE_3 src1_sel:DWORD
	v_and_b32_e32 v8, 0xff, v204
	v_bfe_u32 v9, v204, 16, 8
	v_lshl_add_u32 v8, v8, 2, v6
	v_lshl_add_u32 v9, v9, 2, v6
	s_mov_b64 exec, s[38:39]
	ds_add_u32 v8, v224
	s_mov_b64 exec, s[0:1]
	ds_add_u32 v9, v224
	s_mov_b64 exec, vcc
	v_cmp_eq_u32_sdwa s[38:39], v205, v4 src0_sel:BYTE_1 src1_sel:DWORD
	v_cmp_eq_u32_sdwa s[0:1], v205, v4 src0_sel:BYTE_3 src1_sel:DWORD
	v_and_b32_e32 v8, 0xff, v205
	v_bfe_u32 v9, v205, 16, 8
	v_lshl_add_u32 v8, v8, 2, v6
	v_lshl_add_u32 v9, v9, 2, v6
	s_mov_b64 exec, s[38:39]
	ds_add_u32 v8, v224
	s_mov_b64 exec, s[0:1]
	ds_add_u32 v9, v224
	s_mov_b64 exec, vcc
	v_cmp_eq_u32_sdwa s[38:39], v206, v4 src0_sel:BYTE_1 src1_sel:DWORD
	v_cmp_eq_u32_sdwa s[0:1], v206, v4 src0_sel:BYTE_3 src1_sel:DWORD
	v_and_b32_e32 v8, 0xff, v206
	v_bfe_u32 v9, v206, 16, 8
	v_lshl_add_u32 v8, v8, 2, v6
	v_lshl_add_u32 v9, v9, 2, v6
	s_mov_b64 exec, s[38:39]
	ds_add_u32 v8, v224
	s_mov_b64 exec, s[0:1]
	ds_add_u32 v9, v224
	s_mov_b64 exec, vcc
	v_cmp_eq_u32_sdwa s[38:39], v207, v4 src0_sel:BYTE_1 src1_sel:DWORD
	v_cmp_eq_u32_sdwa s[0:1], v207, v4 src0_sel:BYTE_3 src1_sel:DWORD
	v_and_b32_e32 v8, 0xff, v207
	v_bfe_u32 v9, v207, 16, 8
	v_lshl_add_u32 v8, v8, 2, v6
	v_lshl_add_u32 v9, v9, 2, v6
	s_mov_b64 exec, s[38:39]
	ds_add_u32 v8, v224
	s_mov_b64 exec, s[0:1]
	ds_add_u32 v9, v224
	s_mov_b64 exec, vcc
	s_cmp_gt_i32 s37, s24
	s_cbranch_scc1 .Lpb_done
	v_cmp_eq_u32_sdwa s[38:39], v200, v4 src0_sel:BYTE_1 src1_sel:DWORD
	v_cmp_eq_u32_sdwa s[0:1], v200, v4 src0_sel:BYTE_3 src1_sel:DWORD
	v_and_b32_e32 v8, 0xff, v200
	v_bfe_u32 v9, v200, 16, 8
	v_lshl_add_u32 v8, v8, 2, v6
	v_lshl_add_u32 v9, v9, 2, v6
	s_mov_b64 exec, s[38:39]
	ds_add_u32 v8, v224
	s_mov_b64 exec, s[0:1]
	ds_add_u32 v9, v224
	s_mov_b64 exec, vcc
	v_cmp_eq_u32_sdwa s[38:39], v201, v4 src0_sel:BYTE_1 src1_sel:DWORD
	v_cmp_eq_u32_sdwa s[0:1], v201, v4 src0_sel:BYTE_3 src1_sel:DWORD
	v_and_b32_e32 v8, 0xff, v201
	v_bfe_u32 v9, v201, 16, 8
	v_lshl_add_u32 v8, v8, 2, v6
	v_lshl_add_u32 v9, v9, 2, v6
	s_mov_b64 exec, s[38:39]
	ds_add_u32 v8, v224
	s_mov_b64 exec, s[0:1]
	ds_add_u32 v9, v224
	s_mov_b64 exec, vcc
	v_cmp_eq_u32_sdwa s[38:39], v202, v4 src0_sel:BYTE_1 src1_sel:DWORD
	v_cmp_eq_u32_sdwa s[0:1], v202, v4 src0_sel:BYTE_3 src1_sel:DWORD
	v_and_b32_e32 v8, 0xff, v202
	v_bfe_u32 v9, v202, 16, 8
	v_lshl_add_u32 v8, v8, 2, v6
	v_lshl_add_u32 v9, v9, 2, v6
	s_mov_b64 exec, s[38:39]
	ds_add_u32 v8, v224
	s_mov_b64 exec, s[0:1]
	ds_add_u32 v9, v224
	s_mov_b64 exec, vcc
	v_cmp_eq_u32_sdwa s[38:39], v203, v4 src0_sel:BYTE_1 src1_sel:DWORD
	v_cmp_eq_u32_sdwa s[0:1], v203, v4 src0_sel:BYTE_3 src1_sel:DWORD
	v_and_b32_e32 v8, 0xff, v203
	v_bfe_u32 v9, v203, 16, 8
	v_lshl_add_u32 v8, v8, 2, v6
	v_lshl_add_u32 v9, v9, 2, v6
	s_mov_b64 exec, s[38:39]
	ds_add_u32 v8, v224
	s_mov_b64 exec, s[0:1]
	ds_add_u32 v9, v224
	s_mov_b64 exec, vcc
	v_cmp_eq_u32_sdwa s[38:39], v196, v4 src0_sel:BYTE_1 src1_sel:DWORD
	v_cmp_eq_u32_sdwa s[0:1], v196, v4 src0_sel:BYTE_3 src1_sel:DWORD
	v_and_b32_e32 v8, 0xff, v196
	v_bfe_u32 v9, v196, 16, 8
	v_lshl_add_u32 v8, v8, 2, v6
	v_lshl_add_u32 v9, v9, 2, v6
	s_mov_b64 exec, s[38:39]
	ds_add_u32 v8, v224
	s_mov_b64 exec, s[0:1]
	ds_add_u32 v9, v224
	s_mov_b64 exec, vcc
	v_cmp_eq_u32_sdwa s[38:39], v197, v4 src0_sel:BYTE_1 src1_sel:DWORD
	v_cmp_eq_u32_sdwa s[0:1], v197, v4 src0_sel:BYTE_3 src1_sel:DWORD
	v_and_b32_e32 v8, 0xff, v197
	v_bfe_u32 v9, v197, 16, 8
	v_lshl_add_u32 v8, v8, 2, v6
	v_lshl_add_u32 v9, v9, 2, v6
	s_mov_b64 exec, s[38:39]
	ds_add_u32 v8, v224
	s_mov_b64 exec, s[0:1]
	ds_add_u32 v9, v224
	s_mov_b64 exec, vcc
	v_cmp_eq_u32_sdwa s[38:39], v198, v4 src0_sel:BYTE_1 src1_sel:DWORD
	v_cmp_eq_u32_sdwa s[0:1], v198, v4 src0_sel:BYTE_3 src1_sel:DWORD
	v_and_b32_e32 v8, 0xff, v198
	v_bfe_u32 v9, v198, 16, 8
	v_lshl_add_u32 v8, v8, 2, v6
	v_lshl_add_u32 v9, v9, 2, v6
	s_mov_b64 exec, s[38:39]
	ds_add_u32 v8, v224
	s_mov_b64 exec, s[0:1]
	ds_add_u32 v9, v224
	s_mov_b64 exec, vcc
	v_cmp_eq_u32_sdwa s[38:39], v199, v4 src0_sel:BYTE_1 src1_sel:DWORD
	v_cmp_eq_u32_sdwa s[0:1], v199, v4 src0_sel:BYTE_3 src1_sel:DWORD
	v_and_b32_e32 v8, 0xff, v199
	v_bfe_u32 v9, v199, 16, 8
	v_lshl_add_u32 v8, v8, 2, v6
	v_lshl_add_u32 v9, v9, 2, v6
	s_mov_b64 exec, s[38:39]
	ds_add_u32 v8, v224
	s_mov_b64 exec, s[0:1]
	ds_add_u32 v9, v224
	s_mov_b64 exec, vcc
	s_cmp_gt_i32 s37, s25
	s_cbranch_scc1 .Lpb_done
	v_cmp_eq_u32_sdwa s[38:39], v192, v4 src0_sel:BYTE_1 src1_sel:DWORD
	v_cmp_eq_u32_sdwa s[0:1], v192, v4 src0_sel:BYTE_3 src1_sel:DWORD
	v_and_b32_e32 v8, 0xff, v192
	v_bfe_u32 v9, v192, 16, 8
	v_lshl_add_u32 v8, v8, 2, v6
	v_lshl_add_u32 v9, v9, 2, v6
	s_mov_b64 exec, s[38:39]
	ds_add_u32 v8, v224
	s_mov_b64 exec, s[0:1]
	ds_add_u32 v9, v224
	s_mov_b64 exec, vcc
	v_cmp_eq_u32_sdwa s[38:39], v193, v4 src0_sel:BYTE_1 src1_sel:DWORD
	v_cmp_eq_u32_sdwa s[0:1], v193, v4 src0_sel:BYTE_3 src1_sel:DWORD
	v_and_b32_e32 v8, 0xff, v193
	v_bfe_u32 v9, v193, 16, 8
	v_lshl_add_u32 v8, v8, 2, v6
	v_lshl_add_u32 v9, v9, 2, v6
	s_mov_b64 exec, s[38:39]
	ds_add_u32 v8, v224
	s_mov_b64 exec, s[0:1]
	ds_add_u32 v9, v224
	s_mov_b64 exec, vcc
	v_cmp_eq_u32_sdwa s[38:39], v194, v4 src0_sel:BYTE_1 src1_sel:DWORD
	v_cmp_eq_u32_sdwa s[0:1], v194, v4 src0_sel:BYTE_3 src1_sel:DWORD
	v_and_b32_e32 v8, 0xff, v194
	v_bfe_u32 v9, v194, 16, 8
	v_lshl_add_u32 v8, v8, 2, v6
	v_lshl_add_u32 v9, v9, 2, v6
	s_mov_b64 exec, s[38:39]
	ds_add_u32 v8, v224
	s_mov_b64 exec, s[0:1]
	ds_add_u32 v9, v224
	s_mov_b64 exec, vcc
	v_cmp_eq_u32_sdwa s[38:39], v195, v4 src0_sel:BYTE_1 src1_sel:DWORD
	v_cmp_eq_u32_sdwa s[0:1], v195, v4 src0_sel:BYTE_3 src1_sel:DWORD
	v_and_b32_e32 v8, 0xff, v195
	v_bfe_u32 v9, v195, 16, 8
	v_lshl_add_u32 v8, v8, 2, v6
	v_lshl_add_u32 v9, v9, 2, v6
	s_mov_b64 exec, s[38:39]
	ds_add_u32 v8, v224
	s_mov_b64 exec, s[0:1]
	ds_add_u32 v9, v224
	s_mov_b64 exec, vcc
	v_cmp_eq_u32_sdwa s[38:39], v184, v4 src0_sel:BYTE_1 src1_sel:DWORD
	v_cmp_eq_u32_sdwa s[0:1], v184, v4 src0_sel:BYTE_3 src1_sel:DWORD
	v_and_b32_e32 v8, 0xff, v184
	v_bfe_u32 v9, v184, 16, 8
	v_lshl_add_u32 v8, v8, 2, v6
	v_lshl_add_u32 v9, v9, 2, v6
	s_mov_b64 exec, s[38:39]
	ds_add_u32 v8, v224
	s_mov_b64 exec, s[0:1]
	ds_add_u32 v9, v224
	s_mov_b64 exec, vcc
	v_cmp_eq_u32_sdwa s[38:39], v185, v4 src0_sel:BYTE_1 src1_sel:DWORD
	v_cmp_eq_u32_sdwa s[0:1], v185, v4 src0_sel:BYTE_3 src1_sel:DWORD
	v_and_b32_e32 v8, 0xff, v185
	v_bfe_u32 v9, v185, 16, 8
	v_lshl_add_u32 v8, v8, 2, v6
	v_lshl_add_u32 v9, v9, 2, v6
	s_mov_b64 exec, s[38:39]
	ds_add_u32 v8, v224
	s_mov_b64 exec, s[0:1]
	ds_add_u32 v9, v224
	s_mov_b64 exec, vcc
	v_cmp_eq_u32_sdwa s[38:39], v186, v4 src0_sel:BYTE_1 src1_sel:DWORD
	v_cmp_eq_u32_sdwa s[0:1], v186, v4 src0_sel:BYTE_3 src1_sel:DWORD
	v_and_b32_e32 v8, 0xff, v186
	v_bfe_u32 v9, v186, 16, 8
	v_lshl_add_u32 v8, v8, 2, v6
	v_lshl_add_u32 v9, v9, 2, v6
	s_mov_b64 exec, s[38:39]
	ds_add_u32 v8, v224
	s_mov_b64 exec, s[0:1]
	ds_add_u32 v9, v224
	s_mov_b64 exec, vcc
	v_cmp_eq_u32_sdwa s[38:39], v187, v4 src0_sel:BYTE_1 src1_sel:DWORD
	v_cmp_eq_u32_sdwa s[0:1], v187, v4 src0_sel:BYTE_3 src1_sel:DWORD
	v_and_b32_e32 v8, 0xff, v187
	v_bfe_u32 v9, v187, 16, 8
	v_lshl_add_u32 v8, v8, 2, v6
	v_lshl_add_u32 v9, v9, 2, v6
	s_mov_b64 exec, s[38:39]
	ds_add_u32 v8, v224
	s_mov_b64 exec, s[0:1]
	ds_add_u32 v9, v224
	s_mov_b64 exec, vcc
	s_cmp_gt_i32 s37, s27
	s_cbranch_scc1 .Lpb_done
	v_cmp_eq_u32_sdwa s[38:39], v168, v4 src0_sel:BYTE_1 src1_sel:DWORD
	v_cmp_eq_u32_sdwa s[0:1], v168, v4 src0_sel:BYTE_3 src1_sel:DWORD
	v_and_b32_e32 v8, 0xff, v168
	v_bfe_u32 v9, v168, 16, 8
	v_lshl_add_u32 v8, v8, 2, v6
	v_lshl_add_u32 v9, v9, 2, v6
	s_mov_b64 exec, s[38:39]
	ds_add_u32 v8, v224
	s_mov_b64 exec, s[0:1]
	ds_add_u32 v9, v224
	s_mov_b64 exec, vcc
	v_cmp_eq_u32_sdwa s[38:39], v169, v4 src0_sel:BYTE_1 src1_sel:DWORD
	v_cmp_eq_u32_sdwa s[0:1], v169, v4 src0_sel:BYTE_3 src1_sel:DWORD
	v_and_b32_e32 v8, 0xff, v169
	v_bfe_u32 v9, v169, 16, 8
	v_lshl_add_u32 v8, v8, 2, v6
	v_lshl_add_u32 v9, v9, 2, v6
	s_mov_b64 exec, s[38:39]
	ds_add_u32 v8, v224
	s_mov_b64 exec, s[0:1]
	ds_add_u32 v9, v224
	s_mov_b64 exec, vcc
	v_cmp_eq_u32_sdwa s[38:39], v170, v4 src0_sel:BYTE_1 src1_sel:DWORD
	v_cmp_eq_u32_sdwa s[0:1], v170, v4 src0_sel:BYTE_3 src1_sel:DWORD
	v_and_b32_e32 v8, 0xff, v170
	v_bfe_u32 v9, v170, 16, 8
	v_lshl_add_u32 v8, v8, 2, v6
	v_lshl_add_u32 v9, v9, 2, v6
	s_mov_b64 exec, s[38:39]
	ds_add_u32 v8, v224
	s_mov_b64 exec, s[0:1]
	ds_add_u32 v9, v224
	s_mov_b64 exec, vcc
	v_cmp_eq_u32_sdwa s[38:39], v171, v4 src0_sel:BYTE_1 src1_sel:DWORD
	v_cmp_eq_u32_sdwa s[0:1], v171, v4 src0_sel:BYTE_3 src1_sel:DWORD
	v_and_b32_e32 v8, 0xff, v171
	v_bfe_u32 v9, v171, 16, 8
	v_lshl_add_u32 v8, v8, 2, v6
	v_lshl_add_u32 v9, v9, 2, v6
	s_mov_b64 exec, s[38:39]
	ds_add_u32 v8, v224
	s_mov_b64 exec, s[0:1]
	ds_add_u32 v9, v224
	s_mov_b64 exec, vcc
	v_cmp_eq_u32_sdwa s[38:39], v148, v4 src0_sel:BYTE_1 src1_sel:DWORD
	v_cmp_eq_u32_sdwa s[0:1], v148, v4 src0_sel:BYTE_3 src1_sel:DWORD
	v_and_b32_e32 v8, 0xff, v148
	v_bfe_u32 v9, v148, 16, 8
	v_lshl_add_u32 v8, v8, 2, v6
	v_lshl_add_u32 v9, v9, 2, v6
	s_mov_b64 exec, s[38:39]
	ds_add_u32 v8, v224
	s_mov_b64 exec, s[0:1]
	ds_add_u32 v9, v224
	s_mov_b64 exec, vcc
	v_cmp_eq_u32_sdwa s[38:39], v149, v4 src0_sel:BYTE_1 src1_sel:DWORD
	v_cmp_eq_u32_sdwa s[0:1], v149, v4 src0_sel:BYTE_3 src1_sel:DWORD
	v_and_b32_e32 v8, 0xff, v149
	v_bfe_u32 v9, v149, 16, 8
	v_lshl_add_u32 v8, v8, 2, v6
	v_lshl_add_u32 v9, v9, 2, v6
	s_mov_b64 exec, s[38:39]
	ds_add_u32 v8, v224
	s_mov_b64 exec, s[0:1]
	ds_add_u32 v9, v224
	s_mov_b64 exec, vcc
	v_cmp_eq_u32_sdwa s[38:39], v150, v4 src0_sel:BYTE_1 src1_sel:DWORD
	v_cmp_eq_u32_sdwa s[0:1], v150, v4 src0_sel:BYTE_3 src1_sel:DWORD
	v_and_b32_e32 v8, 0xff, v150
	v_bfe_u32 v9, v150, 16, 8
	v_lshl_add_u32 v8, v8, 2, v6
	v_lshl_add_u32 v9, v9, 2, v6
	s_mov_b64 exec, s[38:39]
	ds_add_u32 v8, v224
	s_mov_b64 exec, s[0:1]
	ds_add_u32 v9, v224
	s_mov_b64 exec, vcc
	v_cmp_eq_u32_sdwa s[38:39], v151, v4 src0_sel:BYTE_1 src1_sel:DWORD
	v_cmp_eq_u32_sdwa s[0:1], v151, v4 src0_sel:BYTE_3 src1_sel:DWORD
	v_and_b32_e32 v8, 0xff, v151
	v_bfe_u32 v9, v151, 16, 8
	v_lshl_add_u32 v8, v8, 2, v6
	v_lshl_add_u32 v9, v9, 2, v6
	s_mov_b64 exec, s[38:39]
	ds_add_u32 v8, v224
	s_mov_b64 exec, s[0:1]
	ds_add_u32 v9, v224
	s_mov_b64 exec, vcc
